# MoE weight absmax pass: 64 rows per trip via dwordx2 loads (lane halves take even/odd rows), twice the bytes in flight per wave
# baseline (speedup 1.0000x reference)
; __device__ __forceinline__ void w2_absmax_item(const float* W, unsigned* amax, int item, int lane, bool dry = false) {
;     const int cb = item & 15, kq = item >> 4; float am = 0.f;
; #pragma unroll 1
;     for (int kb = 0; kb < 4; ++kb) { float tv[32];
; #pragma unroll
;         for (int i = 0; i < 32; ++i) tv[i] = W[(size_t)(kq * 128 + kb * 32 + i) * D + cb * 64 + lane];
; #pragma unroll
;         for (int i = 0; i < 32; ++i) am = fmaxf(am, fabsf(tv[i])); }
; #pragma unroll
;     for (int o = 1; o < 64; o <<= 1) am = fmaxf(am, __shfl_xor(am, o));
;     if (lane == 0 && !dry) atomicMax(amax, __float_as_uint(am));
; }
.LBB0_1390:
	s_mul_hi_i32 s6, s24, 0x92492493
	s_add_i32 s6, s6, s24
	s_lshr_b32 s7, s6, 31
	s_ashr_i32 s6, s6, 9
	s_add_i32 s6, s6, s7
	s_mul_i32 s25, s6, 0xfffffc80
	s_add_i32 s25, s25, s24
	s_ashr_i32 s7, s6, 31
	s_cmpk_gt_i32 s25, 0x1bf
	s_cbranch_scc0 .LBB0_1396
	s_lshl_b32 s8, s22, 2
	s_and_b32 s10, s8, 0xf00
	s_mul_i32 s8, s6, 0x1c00
	s_sub_i32 s8, s23, s8
	s_bfe_u32 s92, s8, 0x180007
	s_mul_i32 s12, s6, 0xe00000
	s_lshl_b64 s[8:9], s[92:93], 19
	s_mul_hi_i32 s11, s6, 0xe00000
	s_add_u32 s8, s12, s8
	s_addc_u32 s9, s11, s9
	s_or_b32 s8, s8, s10
	s_mov_b32 s92, 0xa000
	s_mov_b32 s73, 0x8000
	v_lshl_add_u64 v[2:3], v[0:1], 0, s[8:9]
	v_mov_b32_e32 v6, 0
	s_mov_b64 s[8:9], 0
	v_and_b32_e32 v10, 31, v85
	v_lshrrev_b32_e32 v11, 5, v85
	v_lshlrev_b32_e32 v10, 2, v10
	v_mul_u32_u24_e32 v11, 0xf80, v11
	v_add_u32_e32 v10, v10, v11
	v_mov_b32_e32 v11, 0
	v_lshl_add_u64 v[4:5], v[2:3], 0, v[10:11]
	s_mov_b64 s[26:27], 0x2000
.Lpa2_loop:
	global_load_dwordx2 v[166:167], v[4:5], off
	v_lshl_add_u64 v[4:5], v[4:5], 0, s[26:27]
	global_load_dwordx2 v[168:169], v[4:5], off
	v_lshl_add_u64 v[4:5], v[4:5], 0, s[26:27]
	global_load_dwordx2 v[170:171], v[4:5], off
	v_lshl_add_u64 v[4:5], v[4:5], 0, s[26:27]
	global_load_dwordx2 v[172:173], v[4:5], off
	v_lshl_add_u64 v[4:5], v[4:5], 0, s[26:27]
	global_load_dwordx2 v[174:175], v[4:5], off
	v_lshl_add_u64 v[4:5], v[4:5], 0, s[26:27]
	global_load_dwordx2 v[176:177], v[4:5], off
	v_lshl_add_u64 v[4:5], v[4:5], 0, s[26:27]
	global_load_dwordx2 v[178:179], v[4:5], off
	v_lshl_add_u64 v[4:5], v[4:5], 0, s[26:27]
	global_load_dwordx2 v[180:181], v[4:5], off
	v_lshl_add_u64 v[4:5], v[4:5], 0, s[26:27]
	global_load_dwordx2 v[182:183], v[4:5], off
	v_lshl_add_u64 v[4:5], v[4:5], 0, s[26:27]
	global_load_dwordx2 v[184:185], v[4:5], off
	v_lshl_add_u64 v[4:5], v[4:5], 0, s[26:27]
	global_load_dwordx2 v[186:187], v[4:5], off
	v_lshl_add_u64 v[4:5], v[4:5], 0, s[26:27]
	global_load_dwordx2 v[188:189], v[4:5], off
	v_lshl_add_u64 v[4:5], v[4:5], 0, s[26:27]
	global_load_dwordx2 v[190:191], v[4:5], off
	v_lshl_add_u64 v[4:5], v[4:5], 0, s[26:27]
	global_load_dwordx2 v[192:193], v[4:5], off
	v_lshl_add_u64 v[4:5], v[4:5], 0, s[26:27]
	global_load_dwordx2 v[194:195], v[4:5], off
	v_lshl_add_u64 v[4:5], v[4:5], 0, s[26:27]
	global_load_dwordx2 v[196:197], v[4:5], off
	v_lshl_add_u64 v[4:5], v[4:5], 0, s[26:27]
	global_load_dwordx2 v[198:199], v[4:5], off
	v_lshl_add_u64 v[4:5], v[4:5], 0, s[26:27]
	global_load_dwordx2 v[200:201], v[4:5], off
	v_lshl_add_u64 v[4:5], v[4:5], 0, s[26:27]
	global_load_dwordx2 v[202:203], v[4:5], off
	v_lshl_add_u64 v[4:5], v[4:5], 0, s[26:27]
	global_load_dwordx2 v[204:205], v[4:5], off
	v_lshl_add_u64 v[4:5], v[4:5], 0, s[26:27]
	global_load_dwordx2 v[206:207], v[4:5], off
	v_lshl_add_u64 v[4:5], v[4:5], 0, s[26:27]
	global_load_dwordx2 v[208:209], v[4:5], off
	v_lshl_add_u64 v[4:5], v[4:5], 0, s[26:27]
	global_load_dwordx2 v[210:211], v[4:5], off
	v_lshl_add_u64 v[4:5], v[4:5], 0, s[26:27]
	global_load_dwordx2 v[212:213], v[4:5], off
	v_lshl_add_u64 v[4:5], v[4:5], 0, s[26:27]
	global_load_dwordx2 v[214:215], v[4:5], off
	v_lshl_add_u64 v[4:5], v[4:5], 0, s[26:27]
	global_load_dwordx2 v[216:217], v[4:5], off
	v_lshl_add_u64 v[4:5], v[4:5], 0, s[26:27]
	global_load_dwordx2 v[218:219], v[4:5], off
	v_lshl_add_u64 v[4:5], v[4:5], 0, s[26:27]
	global_load_dwordx2 v[220:221], v[4:5], off
	v_lshl_add_u64 v[4:5], v[4:5], 0, s[26:27]
	global_load_dwordx2 v[222:223], v[4:5], off
	v_lshl_add_u64 v[4:5], v[4:5], 0, s[26:27]
	global_load_dwordx2 v[224:225], v[4:5], off
	v_lshl_add_u64 v[4:5], v[4:5], 0, s[26:27]
	global_load_dwordx2 v[226:227], v[4:5], off
	v_lshl_add_u64 v[4:5], v[4:5], 0, s[26:27]
	global_load_dwordx2 v[228:229], v[4:5], off
	v_lshl_add_u64 v[4:5], v[4:5], 0, s[26:27]
	s_add_u32 s8, s8, 0x40000
	s_addc_u32 s9, s9, 0
	s_cmp_lg_u32 s8, 0x80000
	s_waitcnt vmcnt(0)
	v_max3_f32 v6, v6, |v166|, |v167|
	v_max3_f32 v6, v6, |v168|, |v169|
	v_max3_f32 v6, v6, |v170|, |v171|
	v_max3_f32 v6, v6, |v172|, |v173|
	v_max3_f32 v6, v6, |v174|, |v175|
	v_max3_f32 v6, v6, |v176|, |v177|
	v_max3_f32 v6, v6, |v178|, |v179|
	v_max3_f32 v6, v6, |v180|, |v181|
	v_max3_f32 v6, v6, |v182|, |v183|
	v_max3_f32 v6, v6, |v184|, |v185|
	v_max3_f32 v6, v6, |v186|, |v187|
	v_max3_f32 v6, v6, |v188|, |v189|
	v_max3_f32 v6, v6, |v190|, |v191|
	v_max3_f32 v6, v6, |v192|, |v193|
	v_max3_f32 v6, v6, |v194|, |v195|
	v_max3_f32 v6, v6, |v196|, |v197|
	v_max3_f32 v6, v6, |v198|, |v199|
	v_max3_f32 v6, v6, |v200|, |v201|
	v_max3_f32 v6, v6, |v202|, |v203|
	v_max3_f32 v6, v6, |v204|, |v205|
	v_max3_f32 v6, v6, |v206|, |v207|
	v_max3_f32 v6, v6, |v208|, |v209|
	v_max3_f32 v6, v6, |v210|, |v211|
	v_max3_f32 v6, v6, |v212|, |v213|
	v_max3_f32 v6, v6, |v214|, |v215|
	v_max3_f32 v6, v6, |v216|, |v217|
	v_max3_f32 v6, v6, |v218|, |v219|
	v_max3_f32 v6, v6, |v220|, |v221|
	v_max3_f32 v6, v6, |v222|, |v223|
	v_max3_f32 v6, v6, |v224|, |v225|
	v_max3_f32 v6, v6, |v226|, |v227|
	v_max3_f32 v6, v6, |v228|, |v229|
	s_cbranch_scc1 .Lpa2_loop
	v_and_b32_e32 v2, 64, v251
	v_add_u32_e32 v3, 64, v2
	v_xor_b32_e32 v2, 1, v251
	v_cmp_lt_i32_e32 vcc, v2, v3
	v_max_f32_e32 v4, v6, v6
	s_mov_b64 s[10:11], 0
	v_cndmask_b32_e32 v2, v251, v2, vcc
	v_lshlrev_b32_e32 v2, 2, v2
	ds_bpermute_b32 v2, v2, v6
	s_mov_b64 s[8:9], 0
	s_waitcnt lgkmcnt(0)
	v_max_f32_e32 v2, v2, v2
	v_max_f32_e32 v2, v4, v2
	v_xor_b32_e32 v4, 2, v251
	v_cmp_lt_i32_e32 vcc, v4, v3
	s_nop 1
	v_cndmask_b32_e32 v4, v251, v4, vcc
	v_lshlrev_b32_e32 v4, 2, v4
	ds_bpermute_b32 v4, v4, v2
	s_waitcnt lgkmcnt(0)
	v_max_f32_e32 v4, v4, v4
	v_max_f32_e32 v2, v2, v4
	v_xor_b32_e32 v4, 4, v251
	v_cmp_lt_i32_e32 vcc, v4, v3
	s_nop 1
	v_cndmask_b32_e32 v4, v251, v4, vcc
	v_lshlrev_b32_e32 v4, 2, v4
	ds_bpermute_b32 v4, v4, v2
	s_waitcnt lgkmcnt(0)
	v_max_f32_e32 v4, v4, v4
	v_max_f32_e32 v2, v2, v4
	v_xor_b32_e32 v4, 8, v251
	v_cmp_lt_i32_e32 vcc, v4, v3
	s_nop 1
	v_cndmask_b32_e32 v4, v251, v4, vcc
	v_lshlrev_b32_e32 v4, 2, v4
	ds_bpermute_b32 v4, v4, v2
	s_waitcnt lgkmcnt(0)
	v_max_f32_e32 v4, v4, v4
	v_max_f32_e32 v2, v2, v4
	v_xor_b32_e32 v4, 16, v251
	v_cmp_lt_i32_e32 vcc, v4, v3
	s_nop 1
	v_cndmask_b32_e32 v4, v251, v4, vcc
	v_lshlrev_b32_e32 v4, 2, v4
	ds_bpermute_b32 v4, v4, v2
	s_waitcnt lgkmcnt(0)
	v_max_f32_e32 v4, v4, v4
	v_max_f32_e32 v2, v2, v4
	v_xor_b32_e32 v4, 32, v251
	v_cmp_lt_i32_e32 vcc, v4, v3
	s_nop 1
	v_cndmask_b32_e32 v3, v251, v4, vcc
	v_lshlrev_b32_e32 v3, 2, v3
	ds_bpermute_b32 v3, v3, v2
	s_and_saveexec_b64 s[14:15], s[4:5]
	s_xor_b64 s[14:15], exec, s[14:15]
	s_cbranch_execz .LBB0_1395
	s_lshl_b64 s[8:9], s[6:7], 2
	s_add_u32 s12, s1, s8
	s_waitcnt lgkmcnt(0)
	v_max_f32_e32 v3, v3, v3
	v_max_f32_e32 v2, v2, v2
	s_addc_u32 s13, s16, s9
	v_max_f32_e32 v6, v2, v3
	s_mov_b64 s[8:9], exec

; __device__ __forceinline__ void w13_absmax_item(const float* W1, const float* W3, const float* gain, unsigned* amax, int item, int lane, bool dry = false) {
;     const int kq = item & 3, cb = (item >> 2) % (DFF / 64), mat = (item >> 2) / (DFF / 64); const float* W = mat ? W3 : W1; const int j = cb * 64 + lane;
;     float am = 0.f;
; #pragma unroll 1
;     for (int kb = 0; kb < 8; ++kb) { float tv[32];
; #pragma unroll
;         for (int i = 0; i < 32; ++i) tv[i] = W[(size_t)(kq * 256 + kb * 32 + i) * DFF + j];
; #pragma unroll
;         for (int i = 0; i < 32; ++i) am = fmaxf(am, fabsf(tv[i] * gain[kq * 256 + kb * 32 + i])); }
;     if (!dry) atomicMax(amax + 256 * (j >> 7) + (j & 127) + 128 * mat, __float_as_uint(am));
; }
.LBB0_1397:
	v_readlane_b32 s44, v253, 37
	s_lshl_b32 s8, s21, 2
	v_readlane_b32 s50, v253, 43
	v_readlane_b32 s51, v253, 44
	v_readlane_b32 s58, v253, 51
	v_readlane_b32 s59, v253, 52
	s_bfe_u32 s7, s21, 0x20008
	s_and_b32 s8, s8, 0xc00
	s_mov_b64 s[50:51], s[58:59]
	s_add_u32 s12, s50, s8
	s_addc_u32 s14, s51, 0
	s_ashr_i32 s9, s25, 2
	s_mul_i32 s8, s7, 0x380000
	s_mul_hi_i32 s7, s9, 0x92492493
	s_add_i32 s7, s7, s9
	s_lshr_b32 s10, s7, 31
	s_ashr_i32 s7, s7, 5
	s_add_i32 s7, s7, s10
	v_readlane_b32 s45, v253, 38
	v_readlane_b32 s46, v253, 39
	v_readlane_b32 s47, v253, 40
	v_readlane_b32 s48, v253, 41
	v_readlane_b32 s49, v253, 42
	v_readlane_b32 s52, v253, 45
	v_readlane_b32 s53, v253, 46
	v_readlane_b32 s54, v253, 47
	v_readlane_b32 s55, v253, 48
	v_readlane_b32 s56, v253, 49
	v_readlane_b32 s57, v253, 50
	s_mul_i32 s10, s7, 56
	s_sub_i32 s13, s9, s10
	s_add_i32 s9, s9, 55
	v_readlane_b32 s44, v253, 56
	s_cmpk_lt_u32 s9, 0x6f
	v_readlane_b32 s52, v254, 0
	v_readlane_b32 s54, v254, 2
	v_readlane_b32 s53, v254, 1
	v_readlane_b32 s55, v254, 3
	s_cselect_b32 s10, s52, s54
	s_cselect_b32 s9, s53, s55
	s_add_u32 s10, s10, s20
	s_addc_u32 s9, s9, s19
	s_mul_i32 s15, s6, 0xe00000
	s_mul_hi_i32 s11, s6, 0xe00000
	s_add_u32 s8, s15, s8
	s_addc_u32 s11, s11, 0
	v_lshl_or_b32 v2, s13, 6, v85
	s_add_u32 s8, s10, s8
	v_ashrrev_i32_e32 v3, 31, v2
	s_addc_u32 s9, s9, s11
	v_lshl_add_u64 v[4:5], v[2:3], 2, s[8:9]
	s_mov_b64 s[26:27], 0x7000
	v_readlane_b32 s45, v253, 57
	v_readlane_b32 s46, v253, 58
	v_readlane_b32 s47, v253, 59
	v_readlane_b32 s48, v253, 60
	v_readlane_b32 s49, v253, 61
	v_readlane_b32 s50, v253, 62
	v_readlane_b32 s51, v253, 63
	v_readlane_b32 s56, v254, 4
	v_readlane_b32 s57, v254, 5
	v_readlane_b32 s58, v254, 6
	v_readlane_b32 s59, v254, 7
	v_and_b32_e32 v10, 31, v85
	v_lshrrev_b32_e32 v11, 5, v85
	v_lshlrev_b32_e32 v10, 2, v10
	v_mul_u32_u24_e32 v11, 0x3780, v11
	v_add_u32_e32 v10, v10, v11
	v_mov_b32_e32 v11, 0
	v_lshl_add_u64 v[4:5], v[4:5], 0, v[10:11]
	v_mov_b32_e32 v9, 0
	v_mov_b32_e32 v6, 0
	s_mov_b64 s[8:9], 0
.Lpa13_loop:
	s_add_u32 s10, s12, s8
	s_addc_u32 s11, s14, s9
	global_load_dwordx2 v[166:167], v[4:5], off
	v_lshl_add_u64 v[4:5], v[4:5], 0, s[26:27]
	global_load_dwordx2 v[168:169], v[4:5], off
	v_lshl_add_u64 v[4:5], v[4:5], 0, s[26:27]
	global_load_dwordx2 v[170:171], v[4:5], off
	v_lshl_add_u64 v[4:5], v[4:5], 0, s[26:27]
	global_load_dwordx2 v[172:173], v[4:5], off
	v_lshl_add_u64 v[4:5], v[4:5], 0, s[26:27]
	global_load_dwordx2 v[174:175], v[4:5], off
	v_lshl_add_u64 v[4:5], v[4:5], 0, s[26:27]
	global_load_dwordx2 v[176:177], v[4:5], off
	v_lshl_add_u64 v[4:5], v[4:5], 0, s[26:27]
	global_load_dwordx2 v[178:179], v[4:5], off
	v_lshl_add_u64 v[4:5], v[4:5], 0, s[26:27]
	global_load_dwordx2 v[180:181], v[4:5], off
	v_lshl_add_u64 v[4:5], v[4:5], 0, s[26:27]
	global_load_dwordx2 v[182:183], v[4:5], off
	v_lshl_add_u64 v[4:5], v[4:5], 0, s[26:27]
	global_load_dwordx2 v[184:185], v[4:5], off
	v_lshl_add_u64 v[4:5], v[4:5], 0, s[26:27]
	global_load_dwordx2 v[186:187], v[4:5], off
	v_lshl_add_u64 v[4:5], v[4:5], 0, s[26:27]
	global_load_dwordx2 v[188:189], v[4:5], off
	v_lshl_add_u64 v[4:5], v[4:5], 0, s[26:27]
	global_load_dwordx2 v[190:191], v[4:5], off
	v_lshl_add_u64 v[4:5], v[4:5], 0, s[26:27]
	global_load_dwordx2 v[192:193], v[4:5], off
	v_lshl_add_u64 v[4:5], v[4:5], 0, s[26:27]
	global_load_dwordx2 v[194:195], v[4:5], off
	v_lshl_add_u64 v[4:5], v[4:5], 0, s[26:27]
	global_load_dwordx2 v[196:197], v[4:5], off
	v_lshl_add_u64 v[4:5], v[4:5], 0, s[26:27]
	global_load_dwordx2 v[198:199], v[4:5], off
	v_lshl_add_u64 v[4:5], v[4:5], 0, s[26:27]
	global_load_dwordx2 v[200:201], v[4:5], off
	v_lshl_add_u64 v[4:5], v[4:5], 0, s[26:27]
	global_load_dwordx2 v[202:203], v[4:5], off
	v_lshl_add_u64 v[4:5], v[4:5], 0, s[26:27]
	global_load_dwordx2 v[204:205], v[4:5], off
	v_lshl_add_u64 v[4:5], v[4:5], 0, s[26:27]
	global_load_dwordx2 v[206:207], v[4:5], off
	v_lshl_add_u64 v[4:5], v[4:5], 0, s[26:27]
	global_load_dwordx2 v[208:209], v[4:5], off
	v_lshl_add_u64 v[4:5], v[4:5], 0, s[26:27]
	global_load_dwordx2 v[210:211], v[4:5], off
	v_lshl_add_u64 v[4:5], v[4:5], 0, s[26:27]
	global_load_dwordx2 v[212:213], v[4:5], off
	v_lshl_add_u64 v[4:5], v[4:5], 0, s[26:27]
	global_load_dwordx2 v[214:215], v[4:5], off
	v_lshl_add_u64 v[4:5], v[4:5], 0, s[26:27]
	global_load_dwordx2 v[216:217], v[4:5], off
	v_lshl_add_u64 v[4:5], v[4:5], 0, s[26:27]
	global_load_dwordx2 v[218:219], v[4:5], off
	v_lshl_add_u64 v[4:5], v[4:5], 0, s[26:27]
	global_load_dwordx2 v[220:221], v[4:5], off
	v_lshl_add_u64 v[4:5], v[4:5], 0, s[26:27]
	global_load_dwordx2 v[222:223], v[4:5], off
	v_lshl_add_u64 v[4:5], v[4:5], 0, s[26:27]
	global_load_dwordx2 v[224:225], v[4:5], off
	v_lshl_add_u64 v[4:5], v[4:5], 0, s[26:27]
	global_load_dwordx2 v[226:227], v[4:5], off
	v_lshl_add_u64 v[4:5], v[4:5], 0, s[26:27]
	global_load_dwordx2 v[228:229], v[4:5], off
	v_lshl_add_u64 v[4:5], v[4:5], 0, s[26:27]
	global_load_dwordx4 v[114:117], v250, s[10:11] offset:0
	global_load_dwordx4 v[118:121], v250, s[10:11] offset:16
	global_load_dwordx4 v[122:125], v250, s[10:11] offset:32
	global_load_dwordx4 v[126:129], v250, s[10:11] offset:48
	global_load_dwordx4 v[130:133], v250, s[10:11] offset:64
	global_load_dwordx4 v[134:137], v250, s[10:11] offset:80
	global_load_dwordx4 v[138:141], v250, s[10:11] offset:96
	global_load_dwordx4 v[142:145], v250, s[10:11] offset:112
	global_load_dwordx4 v[146:149], v250, s[10:11] offset:128
	global_load_dwordx4 v[150:153], v250, s[10:11] offset:144
	global_load_dwordx4 v[154:157], v250, s[10:11] offset:160
	global_load_dwordx4 v[158:161], v250, s[10:11] offset:176
	global_load_dwordx4 v[56:59], v250, s[10:11] offset:192
	global_load_dwordx4 v[60:63], v250, s[10:11] offset:208
	global_load_dwordx4 v[64:67], v250, s[10:11] offset:224
	global_load_dwordx4 v[68:71], v250, s[10:11] offset:240
	s_add_u32 s8, s8, 0x100
	s_addc_u32 s9, s9, 0
	v_cmp_lt_u32_e32 vcc, 31, v85
	s_cmpk_lg_i32 s8, 0x400
	s_nop 1
	s_waitcnt vmcnt(0)
; __device__ __forceinline__ void w13_absmax_item(const float* W1, const float* W3, const float* gain, unsigned* amax, int item, int lane, bool dry = false) {
;     const int kq = item & 3, cb = (item >> 2) % (DFF / 64), mat = (item >> 2) / (DFF / 64); const float* W = mat ? W3 : W1; const int j = cb * 64 + lane;
;     float am = 0.f;
; #pragma unroll 1
;     for (int kb = 0; kb < 8; ++kb) { float tv[32];
; #pragma unroll
;         for (int i = 0; i < 32; ++i) tv[i] = W[(size_t)(kq * 256 + kb * 32 + i) * DFF + j];
; #pragma unroll
;         for (int i = 0; i < 32; ++i) am = fmaxf(am, fabsf(tv[i] * gain[kq * 256 + kb * 32 + i])); }
;     if (!dry) atomicMax(amax + 256 * (j >> 7) + (j & 127) + 128 * mat, __float_as_uint(am));
; }
	v_cndmask_b32_e32 v114, v114, v115, vcc
	v_cndmask_b32_e32 v116, v116, v117, vcc
	v_cndmask_b32_e32 v118, v118, v119, vcc
	v_cndmask_b32_e32 v120, v120, v121, vcc
	v_cndmask_b32_e32 v122, v122, v123, vcc
	v_cndmask_b32_e32 v124, v124, v125, vcc
	v_cndmask_b32_e32 v126, v126, v127, vcc
	v_cndmask_b32_e32 v128, v128, v129, vcc
	v_cndmask_b32_e32 v130, v130, v131, vcc
	v_cndmask_b32_e32 v132, v132, v133, vcc
	v_cndmask_b32_e32 v134, v134, v135, vcc
	v_cndmask_b32_e32 v136, v136, v137, vcc
	v_cndmask_b32_e32 v138, v138, v139, vcc
	v_cndmask_b32_e32 v140, v140, v141, vcc
	v_cndmask_b32_e32 v142, v142, v143, vcc
	v_cndmask_b32_e32 v144, v144, v145, vcc
	v_cndmask_b32_e32 v146, v146, v147, vcc
	v_cndmask_b32_e32 v148, v148, v149, vcc
	v_cndmask_b32_e32 v150, v150, v151, vcc
	v_cndmask_b32_e32 v152, v152, v153, vcc
	v_cndmask_b32_e32 v154, v154, v155, vcc
	v_cndmask_b32_e32 v156, v156, v157, vcc
	v_cndmask_b32_e32 v158, v158, v159, vcc
	v_cndmask_b32_e32 v160, v160, v161, vcc
	v_cndmask_b32_e32 v56, v56, v57, vcc
	v_cndmask_b32_e32 v58, v58, v59, vcc
	v_cndmask_b32_e32 v60, v60, v61, vcc
	v_cndmask_b32_e32 v62, v62, v63, vcc
	v_cndmask_b32_e32 v64, v64, v65, vcc
	v_cndmask_b32_e32 v66, v66, v67, vcc
	v_cndmask_b32_e32 v68, v68, v69, vcc
	v_cndmask_b32_e32 v70, v70, v71, vcc
	v_mul_f32_e32 v166, v166, v114
	v_mul_f32_e32 v167, v167, v114
	v_mul_f32_e32 v168, v168, v116
	v_mul_f32_e32 v169, v169, v116
	v_mul_f32_e32 v170, v170, v118
	v_mul_f32_e32 v171, v171, v118
	v_mul_f32_e32 v172, v172, v120
	v_mul_f32_e32 v173, v173, v120
	v_mul_f32_e32 v174, v174, v122
	v_mul_f32_e32 v175, v175, v122
	v_mul_f32_e32 v176, v176, v124
	v_mul_f32_e32 v177, v177, v124
	v_mul_f32_e32 v178, v178, v126
	v_mul_f32_e32 v179, v179, v126
	v_mul_f32_e32 v180, v180, v128
	v_mul_f32_e32 v181, v181, v128
	v_mul_f32_e32 v182, v182, v130
	v_mul_f32_e32 v183, v183, v130
	v_mul_f32_e32 v184, v184, v132
	v_mul_f32_e32 v185, v185, v132
	v_mul_f32_e32 v186, v186, v134
	v_mul_f32_e32 v187, v187, v134
	v_mul_f32_e32 v188, v188, v136
	v_mul_f32_e32 v189, v189, v136
	v_mul_f32_e32 v190, v190, v138
	v_mul_f32_e32 v191, v191, v138
	v_mul_f32_e32 v192, v192, v140
	v_mul_f32_e32 v193, v193, v140
	v_mul_f32_e32 v194, v194, v142
	v_mul_f32_e32 v195, v195, v142
	v_mul_f32_e32 v196, v196, v144
	v_mul_f32_e32 v197, v197, v144
	v_mul_f32_e32 v198, v198, v146
	v_mul_f32_e32 v199, v199, v146
	v_mul_f32_e32 v200, v200, v148
	v_mul_f32_e32 v201, v201, v148
	v_mul_f32_e32 v202, v202, v150
	v_mul_f32_e32 v203, v203, v150
	v_mul_f32_e32 v204, v204, v152
	v_mul_f32_e32 v205, v205, v152
	v_mul_f32_e32 v206, v206, v154
	v_mul_f32_e32 v207, v207, v154
	v_mul_f32_e32 v208, v208, v156
	v_mul_f32_e32 v209, v209, v156
	v_mul_f32_e32 v210, v210, v158
	v_mul_f32_e32 v211, v211, v158
	v_mul_f32_e32 v212, v212, v160
	v_mul_f32_e32 v213, v213, v160
	v_mul_f32_e32 v214, v214, v56
	v_mul_f32_e32 v215, v215, v56
	v_mul_f32_e32 v216, v216, v58
	v_mul_f32_e32 v217, v217, v58
	v_mul_f32_e32 v218, v218, v60
	v_mul_f32_e32 v219, v219, v60
	v_mul_f32_e32 v220, v220, v62
	v_mul_f32_e32 v221, v221, v62
	v_mul_f32_e32 v222, v222, v64
	v_mul_f32_e32 v223, v223, v64
	v_mul_f32_e32 v224, v224, v66
	v_mul_f32_e32 v225, v225, v66
	v_mul_f32_e32 v226, v226, v68
	v_mul_f32_e32 v227, v227, v68
	v_mul_f32_e32 v228, v228, v70
	v_mul_f32_e32 v229, v229, v70
	v_max3_f32 v6, v6, |v166|, |v168|
	v_max3_f32 v9, v9, |v167|, |v169|
	v_max3_f32 v6, v6, |v170|, |v172|
	v_max3_f32 v9, v9, |v171|, |v173|
	v_max3_f32 v6, v6, |v174|, |v176|
	v_max3_f32 v9, v9, |v175|, |v177|
	v_max3_f32 v6, v6, |v178|, |v180|
	v_max3_f32 v9, v9, |v179|, |v181|
	v_max3_f32 v6, v6, |v182|, |v184|
	v_max3_f32 v9, v9, |v183|, |v185|
	v_max3_f32 v6, v6, |v186|, |v188|
	v_max3_f32 v9, v9, |v187|, |v189|
	v_max3_f32 v6, v6, |v190|, |v192|
	v_max3_f32 v9, v9, |v191|, |v193|
	v_max3_f32 v6, v6, |v194|, |v196|
	v_max3_f32 v9, v9, |v195|, |v197|
	v_max3_f32 v6, v6, |v198|, |v200|
	v_max3_f32 v9, v9, |v199|, |v201|
	v_max3_f32 v6, v6, |v202|, |v204|
	v_max3_f32 v9, v9, |v203|, |v205|
	v_max3_f32 v6, v6, |v206|, |v208|
	v_max3_f32 v9, v9, |v207|, |v209|
	v_max3_f32 v6, v6, |v210|, |v212|
	v_max3_f32 v9, v9, |v211|, |v213|
	v_max3_f32 v6, v6, |v214|, |v216|
	v_max3_f32 v9, v9, |v215|, |v217|
	v_max3_f32 v6, v6, |v218|, |v220|
	v_max3_f32 v9, v9, |v219|, |v221|
	v_max3_f32 v6, v6, |v222|, |v224|
	v_max3_f32 v9, v9, |v223|, |v225|
	v_max3_f32 v6, v6, |v226|, |v228|
	v_max3_f32 v9, v9, |v227|, |v229|
	s_cbranch_scc1 .Lpa13_loop
	v_mov_b32_e32 v7, v6
	v_mov_b32_e32 v8, v9
	s_nop 1
	v_permlane32_swap_b32_e32 v6, v7
	v_permlane32_swap_b32_e32 v9, v8
	v_max_f32_e32 v6, v6, v7
	v_max_f32_e32 v9, v9, v8
	v_and_b32_e32 v7, 31, v85
	v_lshlrev_b32_e32 v7, 1, v7
	v_lshl_or_b32 v2, s13, 6, v7
	s_mulk_i32 s6, 0x1c00
	s_add_i32 s8, s6, 0x1c00
	s_ashr_i32 s9, s8, 31
	s_lshl_b64 s[8:9], s[8:9], 2
	s_add_u32 s6, s17, s8
	s_addc_u32 s10, s18, s9
	s_lshl_b32 s8, s13, 7
	s_and_b32 s8, s8, 0xffffff00
	s_ashr_i32 s9, s8, 31
	s_lshl_b64 s[8:9], s[8:9], 2
	s_add_u32 s8, s6, s8
	v_and_b32_e32 v2, 0x7f, v2
	s_addc_u32 s9, s10, s9
	v_lshlrev_b32_e32 v112, 2, v2
	s_lshl_b32 s6, s7, 7
	v_lshl_add_u64 v[2:3], s[8:9], 0, v[112:113]
	s_ashr_i32 s7, s6, 31
	v_lshl_add_u64 v[2:3], s[6:7], 2, v[2:3]
	s_mov_b64 s[8:9], -1
	flat_atomic_umax v[2:3], v9 offset:4
